# v49 with default-policy (non-nt) z stores
# baseline (speedup 1.0000x reference)
.LBB0_148:
	s_ashr_i32 s23, s22, 31
	s_lshl_b64 s[6:7], s[22:23], 10
	s_ashr_i32 s9, s8, 31
	v_lshl_add_u64 v[4:5], v[2:3], 0, s[6:7]
	s_lshl_b64 s[6:7], s[8:9], 10
	s_ashr_i32 s1, s0, 31
	v_lshl_add_u64 v[6:7], v[2:3], 0, s[6:7]
	s_lshl_b64 s[6:7], s[0:1], 10
	s_ashr_i32 s5, s4, 31
	global_load_dwordx4 v[14:17], v[4:5], off
	global_load_dwordx4 v[10:13], v[6:7], off
	v_lshl_add_u64 v[20:21], v[2:3], 0, s[6:7]
	s_lshl_b64 s[6:7], s[4:5], 10
	v_lshl_add_u64 v[22:23], v[2:3], 0, s[6:7]
	global_load_dwordx4 v[6:9], v[20:21], off
	global_load_dwordx4 v[2:5], v[22:23], off
	s_mul_i32 s1, s17, 0x1020
	v_mov_b32_e32 v19, 0
	v_lshl_add_u32 v1, v1, 2, s1
	v_lshl_add_u64 v[20:21], s[20:21], 0, v[18:19]
	v_add_u32_e32 v18, 8, v1
	v_add_u32_e32 v22, 16, v1
	ds_read2st64_b32 v[36:37], v1 offset1:1
	ds_read2st64_b32 v[34:35], v1 offset0:2 offset1:3
	v_add_u32_e32 v1, 24, v1
	ds_read2st64_b32 v[32:33], v18 offset0:4 offset1:5
	ds_read2st64_b32 v[30:31], v18 offset0:6 offset1:7
	ds_read2st64_b32 v[28:29], v22 offset0:8 offset1:9
	ds_read2st64_b32 v[26:27], v22 offset0:10 offset1:11
	ds_read2st64_b32 v[24:25], v1 offset0:12 offset1:13
	ds_read2st64_b32 v[22:23], v1 offset0:14 offset1:15
	s_lshl_b32 s5, s18, 9
	s_or_b32 s1, s5, s28
	s_waitcnt lgkmcnt(7)
	v_add_f32_e64 v1, |v36|, |v37|
	s_mov_b32 s7, 0
	s_add_i32 s6, s1, s29
	s_waitcnt lgkmcnt(6)
	v_add_f32_e64 v1, |v34|, v1
	s_lshl_b64 s[18:19], s[6:7], 10
	v_add_f32_e64 v1, |v35|, v1
	v_lshl_add_u64 v[42:43], v[20:21], 0, s[18:19]
	v_cmp_lt_f32_e32 vcc, 0, v1
	s_waitcnt vmcnt(3)
	v_pk_add_f32 v[38:39], v[14:15], v[36:37] neg_lo:[0,1] neg_hi:[0,1]
	v_pk_add_f32 v[40:41], v[16:17], v[34:35] neg_lo:[0,1] neg_hi:[0,1]
	v_pk_add_f32 v[38:39], v[36:37], v[38:39]
	v_pk_add_f32 v[40:41], v[34:35], v[40:41]
	global_store_dwordx4 v[42:43], v[38:41], off
	s_cbranch_vccz .LBB0_150
	v_pk_add_f32 v[14:15], v[36:37], v[14:15] neg_lo:[0,1] neg_hi:[0,1]
	v_pk_add_f32 v[16:17], v[34:35], v[16:17] neg_lo:[0,1] neg_hi:[0,1]
	v_pk_mul_f32 v[14:15], v[14:15], v[14:15]
	v_pk_mul_f32 v[16:17], v[16:17], v[16:17]
	v_add_f32_e32 v1, v14, v15
	v_add_f32_e32 v1, v1, v16
	v_add_f32_e32 v19, v1, v17
	s_mov_b32 s7, 1
.LBB0_150:
	s_and_saveexec_b64 s[18:19], s[2:3]
	s_lshl_b32 s5, s29, 2
	s_add_i32 s5, s5, 0x11160
	v_mov_b32_e32 v1, s5
	v_mov_b32_e32 v14, s22
	ds_write_b32 v1, v14
	s_or_b64 exec, exec, s[18:19]
	s_or_b32 s5, s29, 1
	s_waitcnt lgkmcnt(5)
	v_add_f32_e64 v1, |v32|, |v33|
	s_add_i32 s18, s1, s5
	s_mov_b32 s19, 0
	s_waitcnt lgkmcnt(4)
	v_add_f32_e64 v1, |v30|, v1
	s_waitcnt vmcnt(3)
	v_pk_add_f32 v[14:15], v[10:11], v[32:33] neg_lo:[0,1] neg_hi:[0,1]
	v_pk_add_f32 v[16:17], v[12:13], v[30:31] neg_lo:[0,1] neg_hi:[0,1]
	s_lshl_b64 s[18:19], s[18:19], 10
	v_add_f32_e64 v1, |v31|, v1
	v_pk_add_f32 v[14:15], v[32:33], v[14:15]
	v_pk_add_f32 v[16:17], v[30:31], v[16:17]
	v_lshl_add_u64 v[34:35], v[20:21], 0, s[18:19]
	v_cmp_lt_f32_e32 vcc, 0, v1
	global_store_dwordx4 v[34:35], v[14:17], off
	s_cbranch_vccz .LBB0_154
	v_pk_add_f32 v[10:11], v[32:33], v[10:11] neg_lo:[0,1] neg_hi:[0,1]
	v_pk_add_f32 v[12:13], v[30:31], v[12:13] neg_lo:[0,1] neg_hi:[0,1]
	v_pk_mul_f32 v[10:11], v[10:11], v[10:11]
	v_pk_mul_f32 v[12:13], v[12:13], v[12:13]
	v_add_f32_e32 v1, v10, v11
	v_add_f32_e32 v1, v1, v12
	v_add_f32_e32 v1, v1, v13
	v_add_f32_e32 v19, v19, v1
	s_add_i32 s7, s7, 1
.LBB0_154:
	s_and_saveexec_b64 s[18:19], s[2:3]
	s_lshl_b32 s5, s5, 2
	s_add_i32 s5, s5, 0x11160
	v_mov_b32_e32 v1, s5
	v_mov_b32_e32 v10, s8
	ds_write_b32 v1, v10
	s_or_b64 exec, exec, s[18:19]
	s_or_b32 s5, s29, 2
	s_waitcnt lgkmcnt(3)
	v_add_f32_e64 v1, |v28|, |v29|
	s_add_i32 s8, s1, s5
	s_mov_b32 s9, 0
	s_waitcnt lgkmcnt(2)
	v_add_f32_e64 v1, |v26|, v1
	s_waitcnt vmcnt(3)
	v_pk_add_f32 v[10:11], v[6:7], v[28:29] neg_lo:[0,1] neg_hi:[0,1]
	v_pk_add_f32 v[12:13], v[8:9], v[26:27] neg_lo:[0,1] neg_hi:[0,1]
	s_lshl_b64 s[8:9], s[8:9], 10
	v_add_f32_e64 v1, |v27|, v1
	v_pk_add_f32 v[10:11], v[28:29], v[10:11]
	v_pk_add_f32 v[12:13], v[26:27], v[12:13]
	v_lshl_add_u64 v[14:15], v[20:21], 0, s[8:9]
	v_cmp_lt_f32_e32 vcc, 0, v1
	global_store_dwordx4 v[14:15], v[10:13], off
	s_cbranch_vccz .LBB0_158
	v_pk_add_f32 v[6:7], v[28:29], v[6:7] neg_lo:[0,1] neg_hi:[0,1]
	v_pk_add_f32 v[8:9], v[26:27], v[8:9] neg_lo:[0,1] neg_hi:[0,1]
	v_pk_mul_f32 v[6:7], v[6:7], v[6:7]
	v_pk_mul_f32 v[8:9], v[8:9], v[8:9]
	v_add_f32_e32 v1, v6, v7
	v_add_f32_e32 v1, v1, v8
	v_add_f32_e32 v1, v1, v9
	v_add_f32_e32 v19, v19, v1
	s_add_i32 s7, s7, 1
.LBB0_158:
	s_and_saveexec_b64 s[8:9], s[2:3]
	s_lshl_b32 s5, s5, 2
	s_add_i32 s5, s5, 0x11160
	v_mov_b32_e32 v1, s5
	v_mov_b32_e32 v6, s0
	ds_write_b32 v1, v6
	s_or_b64 exec, exec, s[8:9]
	s_or_b32 s5, s29, 3
	s_waitcnt lgkmcnt(1)
	v_add_f32_e64 v1, |v24|, |v25|
	s_add_i32 s0, s1, s5
	s_mov_b32 s1, 0
	s_waitcnt lgkmcnt(0)
	v_add_f32_e64 v1, |v22|, v1
	s_waitcnt vmcnt(3)
	v_pk_add_f32 v[6:7], v[2:3], v[24:25] neg_lo:[0,1] neg_hi:[0,1]
	v_pk_add_f32 v[8:9], v[4:5], v[22:23] neg_lo:[0,1] neg_hi:[0,1]
	s_lshl_b64 s[0:1], s[0:1], 10
	v_add_f32_e64 v1, |v23|, v1
	v_pk_add_f32 v[6:7], v[24:25], v[6:7]
	v_pk_add_f32 v[8:9], v[22:23], v[8:9]
	v_lshl_add_u64 v[10:11], v[20:21], 0, s[0:1]
	v_cmp_lt_f32_e32 vcc, 0, v1
	global_store_dwordx4 v[10:11], v[6:9], off
	s_cbranch_vccz .LBB0_162
	v_pk_add_f32 v[2:3], v[24:25], v[2:3] neg_lo:[0,1] neg_hi:[0,1]
	v_pk_add_f32 v[4:5], v[22:23], v[4:5] neg_lo:[0,1] neg_hi:[0,1]
	v_pk_mul_f32 v[2:3], v[2:3], v[2:3]
	v_pk_mul_f32 v[4:5], v[4:5], v[4:5]
	v_add_f32_e32 v1, v2, v3
	v_add_f32_e32 v1, v1, v4
	v_add_f32_e32 v1, v1, v5
	v_add_f32_e32 v19, v19, v1
	s_add_i32 s7, s7, 1
